# no K prefetch for a next block in the last iteration
# baseline (speedup 1.0000x reference)
.LBB1_13:
	s_waitcnt vmcnt(12)
	v_cvt_pk_f16_f32 v151, v120, v121
	v_cvt_pk_f16_f32 v150, v100, v101
	v_cvt_pk_f16_f32 v149, v98, v99
	v_cvt_pk_f16_f32 v148, v112, v113
	s_add_i32 s24, s57, 1
	s_cmp_lg_u32 s57, 7
	s_waitcnt vmcnt(11)
	v_mfma_f32_32x32x16_f16 v[0:15], v[144:147], v[148:151], v[0:15]
	s_cselect_b32 s59, s24, 7
	s_lshl_b32 s25, s59, 2
	s_and_b32 s25, s25, 56
	s_or_b32 s58, s25, s27
	s_lshl_b32 s25, s55, 5
	s_and_b32 s59, s59, 1
	s_waitcnt vmcnt(10)
	v_mfma_f32_32x32x16_f16 v[16:31], v[140:143], v[148:151], v[16:31]
	v_cvt_pk_f16_f32 v143, v180, v181
	v_cvt_pk_f16_f32 v142, v124, v125
	v_cvt_pk_f16_f32 v141, v122, v123
	v_cvt_pk_f16_f32 v140, v102, v103
	s_waitcnt vmcnt(9)
	s_nop 0
	v_mfma_f32_32x32x16_f16 v[0:15], v[136:139], v[140:143], v[0:15]
	s_waitcnt vmcnt(8)
	v_mfma_f32_32x32x16_f16 v[16:31], v[132:135], v[140:143], v[16:31]
	s_add_i32 s61, s35, s60
	s_and_b32 s61, s61, 0x3f000
	v_or_b32_e32 v144, s61, v248
	s_add_i32 s61, s36, s60
	s_and_b32 s61, s61, 0x3f000
	v_or_b32_e32 v160, s61, v248
	global_load_dwordx4 v[132:135], v144, s[16:17]
	global_load_dwordx4 v[136:139], v144, s[16:17] offset:1024
	global_load_dwordx4 v[140:143], v144, s[16:17] offset:2048
	s_nop 0
	global_load_dwordx4 v[144:147], v144, s[16:17] offset:3072
	s_nop 0
	global_load_dwordx4 v[148:151], v160, s[16:17]
	global_load_dwordx4 v[152:155], v160, s[16:17] offset:1024
	global_load_dwordx4 v[156:159], v160, s[16:17] offset:2048
	s_nop 0
	global_load_dwordx4 v[160:163], v160, s[16:17] offset:3072
	v_cvt_pk_f16_f32 v253, v96, v97
	v_cvt_pk_f16_f32 v252, v84, v85
	v_cvt_pk_f16_f32 v251, v82, v83
	v_cvt_pk_f16_f32 v250, v80, v81
	s_waitcnt vmcnt(15)
	s_nop 0
	v_mfma_f32_32x32x16_f16 v[0:15], v[60:63], v[250:253], v[0:15]
	s_waitcnt vmcnt(14)
	v_mfma_f32_32x32x16_f16 v[16:31], v[56:59], v[250:253], v[16:31]
	v_cvt_pk_f16_f32 v59, v94, v95
	v_cvt_pk_f16_f32 v58, v90, v91
	v_cvt_pk_f16_f32 v57, v88, v89
	v_cvt_pk_f16_f32 v56, v86, v87
	s_waitcnt vmcnt(13)
	s_nop 0
	v_mfma_f32_32x32x16_f16 v[0:15], v[52:55], v[56:59], v[0:15]
	s_waitcnt vmcnt(12)
	v_mfma_f32_32x32x16_f16 v[16:31], v[48:51], v[56:59], v[16:31]
	v_cvt_pk_f16_f32 v51, v176, v177
	v_cvt_pk_f16_f32 v50, v110, v111
	v_cvt_pk_f16_f32 v49, v108, v109
	v_cvt_pk_f16_f32 v48, v92, v93
	s_waitcnt vmcnt(11)
	s_nop 0
	v_mfma_f32_32x32x16_f16 v[0:15], v[44:47], v[48:51], v[0:15]
	s_waitcnt vmcnt(10)
	v_mfma_f32_32x32x16_f16 v[16:31], v[40:43], v[48:51], v[16:31]
	v_cvt_pk_f16_f32 v43, v206, v207
	v_cvt_pk_f16_f32 v42, v194, v195
	v_cvt_pk_f16_f32 v41, v192, v193
	v_cvt_pk_f16_f32 v40, v174, v175
	s_waitcnt vmcnt(9)
	s_nop 0
	v_mfma_f32_32x32x16_f16 v[0:15], v[36:39], v[40:43], v[0:15]
	s_waitcnt vmcnt(8)
	v_mfma_f32_32x32x16_f16 v[16:31], v[32:35], v[40:43], v[16:31]
	s_add_i32 s61, s37, s60
	s_add_i32 s60, s38, s60
	s_and_b32 s61, s61, 0x3f000
	s_and_b32 s60, s60, 0x3f000
	v_or_b32_e32 v44, s61, v248
	v_or_b32_e32 v60, s60, v248
	global_load_dwordx4 v[32:35], v44, s[16:17]
	global_load_dwordx4 v[36:39], v44, s[16:17] offset:1024
	global_load_dwordx4 v[40:43], v44, s[16:17] offset:2048
	s_nop 0
	global_load_dwordx4 v[44:47], v44, s[16:17] offset:3072
	s_nop 0
	global_load_dwordx4 v[48:51], v60, s[16:17]
	global_load_dwordx4 v[52:55], v60, s[16:17] offset:1024
	global_load_dwordx4 v[56:59], v60, s[16:17] offset:2048
	s_nop 0
	global_load_dwordx4 v[60:63], v60, s[16:17] offset:3072
	v_cvt_pk_f16_f32 v251, v74, v75
	v_cvt_pk_f16_f32 v250, v68, v69
	v_cvt_pk_f16_f32 v249, v66, v67
	v_cvt_pk_f16_f32 v248, v64, v65
	s_waitcnt vmcnt(15)
	s_nop 0
	v_mfma_f32_32x32x16_f16 v[0:15], v[132:135], v[248:251], v[0:15]
	v_cvt_pk_f16_f32 v135, v172, v173
	v_cvt_pk_f16_f32 v134, v106, v107
	v_cvt_pk_f16_f32 v133, v104, v105
	v_cvt_pk_f16_f32 v132, v72, v73
	s_waitcnt vmcnt(14)
	v_mfma_f32_32x32x16_f16 v[16:31], v[136:139], v[248:251], v[16:31]
	s_waitcnt vmcnt(13)
	v_mfma_f32_32x32x16_f16 v[0:15], v[140:143], v[132:135], v[0:15]
	s_waitcnt vmcnt(12)
	v_mfma_f32_32x32x16_f16 v[16:31], v[144:147], v[132:135], v[16:31]
	v_cvt_pk_f16_f32 v135, v202, v203
	v_cvt_pk_f16_f32 v134, v190, v191
	v_cvt_pk_f16_f32 v133, v188, v189
	v_cvt_pk_f16_f32 v132, v170, v171
	s_waitcnt vmcnt(11)
	s_nop 0
	v_mfma_f32_32x32x16_f16 v[0:15], v[148:151], v[132:135], v[0:15]
	s_waitcnt vmcnt(10)
	v_mfma_f32_32x32x16_f16 v[16:31], v[152:155], v[132:135], v[16:31]
	v_cvt_pk_f16_f32 v135, v222, v223
	v_cvt_pk_f16_f32 v134, v216, v217
	v_cvt_pk_f16_f32 v133, v214, v215
	v_cvt_pk_f16_f32 v132, v200, v201
	s_waitcnt vmcnt(9)
	s_nop 0
	v_mfma_f32_32x32x16_f16 v[0:15], v[156:159], v[132:135], v[0:15]
	s_waitcnt vmcnt(8)
	v_mfma_f32_32x32x16_f16 v[16:31], v[160:163], v[132:135], v[16:31]
	v_cvt_pk_f16_f32 v135, v168, v169
	v_cvt_pk_f16_f32 v134, v78, v79
	v_cvt_pk_f16_f32 v133, v76, v77
	v_cvt_pk_f16_f32 v132, v70, v71
	s_waitcnt vmcnt(7)
	s_nop 0
	v_mfma_f32_32x32x16_f16 v[0:15], v[32:35], v[132:135], v[0:15]
	v_cvt_pk_f16_f32 v35, v198, v199
	v_cvt_pk_f16_f32 v34, v186, v187
	v_cvt_pk_f16_f32 v33, v184, v185
	v_cvt_pk_f16_f32 v32, v126, v127
	s_waitcnt vmcnt(6)
	v_mfma_f32_32x32x16_f16 v[16:31], v[36:39], v[132:135], v[16:31]
	s_waitcnt vmcnt(5)
	v_mfma_f32_32x32x16_f16 v[0:15], v[40:43], v[32:35], v[0:15]
	s_waitcnt vmcnt(4)
	v_mfma_f32_32x32x16_f16 v[16:31], v[44:47], v[32:35], v[16:31]
	v_cvt_pk_f16_f32 v35, v220, v221
	v_cvt_pk_f16_f32 v34, v212, v213
	v_cvt_pk_f16_f32 v33, v210, v211
	v_cvt_pk_f16_f32 v32, v196, v197
	s_waitcnt vmcnt(3)
	s_nop 0
	v_mfma_f32_32x32x16_f16 v[0:15], v[48:51], v[32:35], v[0:15]
	s_waitcnt vmcnt(2)
	v_mfma_f32_32x32x16_f16 v[16:31], v[52:55], v[32:35], v[16:31]
	v_cvt_pk_f16_f32 v35, v228, v229
	v_cvt_pk_f16_f32 v34, v226, v227
	v_cvt_pk_f16_f32 v33, v224, v225
	v_cvt_pk_f16_f32 v32, v218, v219
	s_waitcnt vmcnt(1)
	s_nop 0
	v_mfma_f32_32x32x16_f16 v[0:15], v[56:59], v[32:35], v[0:15]
	s_waitcnt vmcnt(0)
	v_mfma_f32_32x32x16_f16 v[16:31], v[60:63], v[32:35], v[16:31]
	s_cmp_eq_u32 s12, 28
	s_cbranch_scc1 .Lka_late
	s_cmp_lt_u32 s31, 0x200
	s_cbranch_scc0 .Lka_late
	s_or_b32 s62, s39, s59
	s_lshl_b32 s62, s62, 12
	s_lshl_b32 s66, s58, 18
	s_and_b32 s63, s62, 0x3f000
	s_or_b32 s63, s63, s66
	v_or_b32_e32 v252, s63, v231
	global_load_dwordx4 v[48:51], v252, s[6:7]
	global_load_dwordx4 v[52:55], v252, s[6:7] offset:1024
	global_load_dwordx4 v[56:59], v252, s[6:7] offset:2048
	global_load_dwordx4 v[60:63], v252, s[6:7] offset:3072
	s_add_i32 s63, s62, 0x4000
	s_and_b32 s63, s63, 0x3f000
	s_or_b32 s63, s63, s66
	v_or_b32_e32 v253, s63, v231
	global_load_dwordx4 v[40:43], v253, s[6:7] offset:2048
	global_load_dwordx4 v[44:47], v253, s[6:7] offset:3072
	s_add_i32 s63, s62, 0x6000
	s_and_b32 s63, s63, 0x3f000
	s_or_b32 s63, s63, s66
	v_or_b32_e32 v252, s63, v231
	global_load_dwordx4 v[148:151], v252, s[6:7] offset:3072
	s_add_i32 s63, s62, 0x7000
	s_and_b32 s63, s63, 0x3f000
	s_or_b32 s63, s63, s66
	v_or_b32_e32 v253, s63, v231
	global_load_dwordx4 v[132:135], v253, s[6:7]
	global_load_dwordx4 v[136:139], v253, s[6:7] offset:1024
	global_load_dwordx4 v[140:143], v253, s[6:7] offset:2048
	global_load_dwordx4 v[144:147], v253, s[6:7] offset:3072
	s_add_i32 s63, s62, 0x1000
	s_and_b32 s63, s63, 0x3f000
	s_or_b32 s63, s63, s66
	v_or_b32_e32 v252, s63, v231
	global_load_dwordx4 v[152:155], v252, s[6:7]
	global_load_dwordx4 v[156:159], v252, s[6:7] offset:1024
.Lka_late:
	s_nop 9
	v_mul_f32_e64 v0, s18, v0
	v_mul_f32_e64 v1, s19, v1
	v_mul_f32_e64 v2, s18, v2
	v_mul_f32_e64 v3, s19, v3
	v_pk_mul_f32 v[16:17], s[18:19], v[16:17]
	v_pk_mul_f32 v[18:19], s[18:19], v[18:19]
	ds_write_b128 v164, v[0:3]
	ds_write_b128 v164, v[16:19] offset:128
	v_pk_mul_f32 v[0:1], s[18:19], v[4:5]
	v_pk_mul_f32 v[2:3], s[18:19], v[6:7]
	v_pk_mul_f32 v[4:5], s[18:19], v[20:21]
	v_pk_mul_f32 v[6:7], s[18:19], v[22:23]
	ds_write_b128 v164, v[0:3] offset:32
	ds_write_b128 v164, v[4:7] offset:160
	v_pk_mul_f32 v[0:1], s[18:19], v[8:9]
	v_pk_mul_f32 v[2:3], s[18:19], v[10:11]
	v_pk_mul_f32 v[4:5], s[18:19], v[24:25]
	v_pk_mul_f32 v[6:7], s[18:19], v[26:27]
	ds_write_b128 v164, v[0:3] offset:64
	ds_write_b128 v164, v[4:7] offset:192
	v_pk_mul_f32 v[0:1], s[18:19], v[12:13]
	v_pk_mul_f32 v[2:3], s[18:19], v[14:15]
	v_pk_mul_f32 v[4:5], s[18:19], v[28:29]
	v_pk_mul_f32 v[6:7], s[18:19], v[30:31]
	ds_write_b128 v164, v[0:3] offset:96
	ds_write_b128 v164, v[4:7] offset:224
	s_waitcnt lgkmcnt(0)
	s_barrier
	s_cmp_eq_u32 s12, 28
	s_cbranch_scc1 .Lka_done
	s_cmp_lt_u32 s31, 0x200
	s_cbranch_scc1 .Lka_done
	s_or_b32 s62, s39, s59
	s_lshl_b32 s62, s62, 12
	s_lshl_b32 s66, s58, 18
	s_and_b32 s63, s62, 0x3f000
	s_or_b32 s63, s63, s66
	v_or_b32_e32 v252, s63, v231
	global_load_dwordx4 v[48:51], v252, s[6:7]
	global_load_dwordx4 v[52:55], v252, s[6:7] offset:1024
	global_load_dwordx4 v[56:59], v252, s[6:7] offset:2048
	global_load_dwordx4 v[60:63], v252, s[6:7] offset:3072
	s_add_i32 s63, s62, 0x4000
	s_and_b32 s63, s63, 0x3f000
	s_or_b32 s63, s63, s66
	v_or_b32_e32 v253, s63, v231
	global_load_dwordx4 v[40:43], v253, s[6:7] offset:2048
	global_load_dwordx4 v[44:47], v253, s[6:7] offset:3072
	s_add_i32 s63, s62, 0x6000
	s_and_b32 s63, s63, 0x3f000
	s_or_b32 s63, s63, s66
	v_or_b32_e32 v252, s63, v231
	global_load_dwordx4 v[148:151], v252, s[6:7] offset:3072
	s_add_i32 s63, s62, 0x7000
	s_and_b32 s63, s63, 0x3f000
	s_or_b32 s63, s63, s66
	v_or_b32_e32 v253, s63, v231
	global_load_dwordx4 v[132:135], v253, s[6:7]
	global_load_dwordx4 v[136:139], v253, s[6:7] offset:1024
	global_load_dwordx4 v[140:143], v253, s[6:7] offset:2048
	global_load_dwordx4 v[144:147], v253, s[6:7] offset:3072
	s_add_i32 s63, s62, 0x1000
	s_and_b32 s63, s63, 0x3f000
	s_or_b32 s63, s63, s66
	v_or_b32_e32 v252, s63, v231
	global_load_dwordx4 v[152:155], v252, s[6:7]
	global_load_dwordx4 v[156:159], v252, s[6:7] offset:1024
.Lka_done:
	ds_read2_b32 v[0:1], v235 offset1:32
	ds_read2_b32 v[2:3], v235 offset0:64 offset1:96
	ds_read2_b32 v[4:5], v235 offset0:128 offset1:160
	ds_read2_b32 v[6:7], v235 offset0:192 offset1:224
	ds_read2_b32 v[10:11], v236 offset0:128 offset1:160
	ds_read2_b32 v[16:17], v165 offset1:32
	ds_write_b128 v232, v[128:131]
	s_waitcnt lgkmcnt(6)
	v_max_f32_e32 v8, v1, v1
	v_max_f32_e32 v9, v0, v0
	v_max_f32_e32 v8, v9, v8
	s_waitcnt lgkmcnt(5)
	v_max3_f32 v8, v8, v2, v3
	s_waitcnt lgkmcnt(4)
	v_max3_f32 v8, v8, v4, v5
	s_waitcnt lgkmcnt(3)
	v_max3_f32 v14, v8, v6, v7
	ds_read2_b32 v[8:9], v236 offset1:32
	v_sub_f32_e32 v0, v0, v14
	v_sub_f32_e32 v1, v1, v14
	v_exp_f32_e32 v0, v0
	v_exp_f32_e32 v1, v1
	v_sub_f32_e32 v4, v4, v14
	v_sub_f32_e32 v5, v5, v14
	v_exp_f32_e32 v4, v4
	v_exp_f32_e32 v5, v5
	s_waitcnt lgkmcnt(0)
	v_pk_mul_f32 v[0:1], v[8:9], v[0:1]
	ds_read2_b32 v[8:9], v236 offset0:64 offset1:96
	v_sub_f32_e32 v2, v2, v14
	v_sub_f32_e32 v3, v3, v14
	v_exp_f32_e32 v2, v2
	v_exp_f32_e32 v3, v3
	ds_read2_b32 v[12:13], v236 offset0:192 offset1:224
	v_sub_f32_e32 v6, v6, v14
	v_sub_f32_e32 v7, v7, v14
	v_pk_mul_f32 v[18:19], v[10:11], v[4:5]
	v_sub_f32_e32 v4, v247, v14
	ds_read2_b32 v[22:23], v165 offset0:64 offset1:96
	ds_read2_b32 v[24:25], v165 offset0:128 offset1:160
	ds_read2_b32 v[26:27], v165 offset0:192 offset1:224
	v_exp_f32_e32 v6, v6
	v_exp_f32_e32 v7, v7
	v_exp_f32_e32 v34, v4
	v_max_f32_e32 v4, v17, v17
	v_max_f32_e32 v5, v16, v16
	v_add_f32_e32 v0, 0, v0
	s_waitcnt lgkmcnt(4)
	v_pk_mul_f32 v[2:3], v[8:9], v[2:3]
	v_max_f32_e32 v4, v5, v4
	v_add_f32_e32 v0, v0, v1
	s_waitcnt lgkmcnt(2)
	v_max3_f32 v4, v4, v22, v23
	v_add_f32_e32 v0, v0, v2
	s_waitcnt lgkmcnt(1)
	v_max3_f32 v4, v4, v24, v25
	v_add_f32_e32 v0, v0, v3
	v_pk_mul_f32 v[20:21], v[12:13], v[6:7]
	s_waitcnt lgkmcnt(0)
	v_max3_f32 v35, v4, v26, v27
	v_add_f32_e32 v18, v0, v18
	ds_read_b128 v[0:3], v245
	ds_read_b128 v[4:7], v237
	v_sub_f32_e32 v8, v16, v35
	v_exp_f32_e32 v16, v8
	ds_read2_b32 v[28:29], v242 offset1:32
	ds_read_b128 v[8:11], v245 offset:34816
	ds_read_b128 v[12:15], v245 offset:60928
	s_min_u32 s57, s57, 5
	s_waitcnt lgkmcnt(3)
	v_pk_add_f32 v[0:1], v[0:1], v[4:5]
	v_pk_add_f32 v[2:3], v[2:3], v[6:7]
	v_pk_fma_f32 v[30:31], v[16:17], v[0:1], 0 op_sel_hi:[0,1,0]
	v_sub_f32_e32 v0, v17, v35
	v_pk_fma_f32 v[32:33], v[16:17], v[2:3], 0 op_sel_hi:[0,1,0]
	v_exp_f32_e32 v17, v0
	v_add_f32_e32 v0, v18, v19
	v_add_f32_e32 v0, v0, v20
	v_add_f32_e32 v36, v0, v21
	ds_read_b128 v[0:3], v245 offset:8704
	ds_read_b128 v[4:7], v245 offset:17408
	s_waitcnt lgkmcnt(4)
	v_pk_mul_f32 v[18:19], v[28:29], v[16:17]
	v_sub_f32_e32 v16, v22, v35
	v_exp_f32_e32 v16, v16
	v_add_f32_e32 v20, 0, v18
	v_mov_b32_e32 v18, v17
	s_waitcnt lgkmcnt(1)
	v_pk_fma_f32 v[0:1], v[18:19], v[0:1], v[30:31] op_sel_hi:[0,1,1]
	v_pk_fma_f32 v[2:3], v[18:19], v[2:3], v[32:33] op_sel_hi:[0,1,1]
	s_waitcnt lgkmcnt(0)
	v_pk_fma_f32 v[4:5], v[16:17], v[4:5], v[0:1] op_sel_hi:[0,1,1]
	v_sub_f32_e32 v0, v23, v35
	v_pk_fma_f32 v[6:7], v[16:17], v[6:7], v[2:3] op_sel_hi:[0,1,1]
	v_exp_f32_e32 v17, v0
	v_add_f32_e32 v21, v20, v19
	ds_read_b128 v[0:3], v245 offset:26112
	ds_read2_b32 v[18:19], v242 offset0:64 offset1:96
	v_sub_f32_e32 v22, v24, v35
	v_exp_f32_e32 v22, v22
	v_mov_b32_e32 v20, v17
	s_waitcnt lgkmcnt(1)
	v_pk_fma_f32 v[0:1], v[20:21], v[0:1], v[4:5] op_sel_hi:[0,1,1]
	v_pk_fma_f32 v[2:3], v[20:21], v[2:3], v[6:7] op_sel_hi:[0,1,1]
	ds_read2_b32 v[4:5], v242 offset0:128 offset1:160
	v_pk_fma_f32 v[8:9], v[22:23], v[8:9], v[0:1] op_sel_hi:[0,1,1]
	v_sub_f32_e32 v0, v25, v35
	v_pk_fma_f32 v[10:11], v[22:23], v[10:11], v[2:3] op_sel_hi:[0,1,1]
	v_exp_f32_e32 v23, v0
	s_waitcnt lgkmcnt(1)
	v_pk_mul_f32 v[0:1], v[18:19], v[16:17]
	s_lshl_b32 s58, s58, 18
	v_add_f32_e32 v0, v21, v0
	v_add_f32_e32 v2, v0, v1
	s_waitcnt lgkmcnt(0)
	v_pk_mul_f32 v[0:1], v[4:5], v[22:23]
	v_sub_f32_e32 v4, v26, v35
	v_add_f32_e32 v0, v2, v0
	v_add_f32_e32 v17, v0, v1
	ds_read_b128 v[0:3], v245 offset:43520
	v_exp_f32_e32 v18, v4
	ds_read2_b32 v[20:21], v242 offset0:192 offset1:224
	v_sub_f32_e32 v4, v27, v35
	v_exp_f32_e32 v19, v4
	ds_read_b128 v[4:7], v245 offset:52224
	v_mov_b32_e32 v16, v23
	s_waitcnt lgkmcnt(2)
	v_pk_fma_f32 v[0:1], v[16:17], v[0:1], v[8:9] op_sel_hi:[0,1,1]
	s_waitcnt lgkmcnt(1)
	v_pk_mul_f32 v[8:9], v[20:21], v[18:19]
	v_pk_fma_f32 v[2:3], v[16:17], v[2:3], v[10:11] op_sel_hi:[0,1,1]
	v_add_f32_e32 v8, v17, v8
	v_add_f32_e32 v8, v8, v9
	s_waitcnt lgkmcnt(0)
	v_pk_fma_f32 v[0:1], v[18:19], v[4:5], v[0:1] op_sel_hi:[0,1,1]
	v_div_scale_f32 v5, s[60:61], v8, v8, 1.0
	v_pk_fma_f32 v[2:3], v[18:19], v[6:7], v[2:3] op_sel_hi:[0,1,1]
	v_rcp_f32_e32 v6, v5
	v_mov_b32_e32 v4, v19
	v_pk_fma_f32 v[2:3], v[4:5], v[14:15], v[2:3] op_sel_hi:[0,1,1]
	v_pk_fma_f32 v[0:1], v[4:5], v[12:13], v[0:1] op_sel_hi:[0,1,1]
	v_fma_f32 v4, -v5, v6, 1.0
	v_fmac_f32_e32 v6, v4, v6
	v_div_scale_f32 v4, vcc, 1.0, v8, 1.0
	v_mul_f32_e32 v7, v4, v6
	v_fma_f32 v9, -v5, v7, v4
	v_fmac_f32_e32 v7, v9, v6
	v_fma_f32 v4, -v5, v7, v4
	v_div_fmas_f32 v4, v4, v6, v7
	s_lshl_b32 s60, s56, 19
	s_lshl_b32 s61, s55, 13
	v_div_fixup_f32 v4, v4, v8, 1.0
	s_add_i32 s60, s60, s61
	v_pk_mul_f32 v[2:3], v[2:3], v[4:5] op_sel_hi:[1,0]
	v_pk_mul_f32 v[0:1], v[0:1], v[4:5] op_sel_hi:[1,0]
	v_or_b32_e32 v4, s60, v230
	s_lshl_b32 s60, s57, 2
	s_add_i32 s60, s60, 8
	s_and_b32 s60, s60, 56
	s_and_b32 s57, s57, 1
	s_or_b32 s60, s60, s27
	s_or_b32 s57, s57, s28
	s_lshl_b32 s60, s60, 19
	s_lshl_b32 s57, s57, 13
	s_add_i32 s60, s60, s57
	s_or_b32 s62, s39, s59
	s_lshl_b32 s62, s62, 12
	global_store_dwordx4 v4, v[0:3], s[8:9] nt
	v_mov_b32_e32 v252, v34
	v_mov_b32_e32 v253, v36
	v_or_b32_e32 v0, s60, v230
	s_barrier
	global_load_dwordx4 v[128:131], v0, s[4:5]
	s_cmp_eq_u32 s12, 28
	s_cbranch_scc1 .Lkb_skip
	s_add_i32 s63, s62, 0x4000
	s_and_b32 s63, s63, 0x3f000
	s_or_b32 s63, s63, s58
	v_or_b32_e32 v2, s63, v231
	global_load_dwordx4 v[32:35], v2, s[6:7]
	global_load_dwordx4 v[36:39], v2, s[6:7] offset:1024
	s_add_i32 s63, s62, 0x5000
	s_and_b32 s63, s63, 0x3f000
	s_or_b32 s63, s63, s58
	v_or_b32_e32 v3, s63, v231
	global_load_dwordx4 v[16:19], v3, s[6:7]
	global_load_dwordx4 v[20:23], v3, s[6:7] offset:1024
	global_load_dwordx4 v[24:27], v3, s[6:7] offset:2048
	global_load_dwordx4 v[28:31], v3, s[6:7] offset:3072
	s_add_i32 s63, s62, 0x6000
	s_and_b32 s63, s63, 0x3f000
	s_or_b32 s63, s63, s58
	v_or_b32_e32 v2, s63, v231
	global_load_dwordx4 v[4:7], v2, s[6:7]
	global_load_dwordx4 v[8:11], v2, s[6:7] offset:1024
	global_load_dwordx4 v[12:15], v2, s[6:7] offset:2048
.Lkb_skip:
	v_div_scale_f32 v1, s[64:65], v253, v253, v252
	v_rcp_f32_e32 v2, v1
	s_nop 0
	v_fma_f32 v0, -v1, v2, 1.0
	v_fmac_f32_e32 v2, v0, v2
	v_div_scale_f32 v0, vcc, v252, v253, v252
	v_mul_f32_e32 v3, v0, v2
	v_fma_f32 v248, -v1, v3, v0
	v_fmac_f32_e32 v3, v248, v2
	v_fma_f32 v0, -v1, v3, v0
	v_div_fmas_f32 v0, v0, v2, v3
	v_div_fixup_f32 v1, v0, v253, v252
	v_mul_f32_e32 v0, s18, v1
	v_mov_b32_e32 v2, s26
	v_mov_b32_e32 v3, s23
	v_cmp_eq_u32_e64 s[64:65], 0, v233
	v_cmp_eq_u32_e64 s[66:67], 1, v233
	v_cmp_eq_u32_e64 s[68:69], 2, v233
	v_cmp_eq_u32_e64 s[70:71], 3, v233
	v_cndmask_b32_e64 v248, v2, v3, s[64:65]
	v_cndmask_b32_e64 v249, v2, v3, s[66:67]
	v_cndmask_b32_e64 v250, v2, v3, s[68:69]
	v_cndmask_b32_e64 v251, v2, v3, s[70:71]
	v_mul_f32_e32 v248, v1, v248
	v_mul_f32_e32 v249, v1, v249
	v_mul_f32_e32 v250, v1, v250
	v_mul_f32_e32 v251, v1, v251
	v_cndmask_b32_e64 v248, v0, v248, s[2:3]
	v_cndmask_b32_e64 v249, v0, v249, s[2:3]
	v_cndmask_b32_e64 v250, v0, v250, s[2:3]
	v_cndmask_b32_e64 v251, v0, v251, s[2:3]
	v_mul_f32_e32 v248, v248, v208
	v_mul_f32_e32 v249, v249, v209
	v_mul_f32_e32 v250, v250, v204
	v_mul_f32_e32 v251, v251, v205
	ds_write_b128 v238, v[248:251]
	v_cmp_eq_u32_e64 s[64:65], 4, v233
	v_cmp_eq_u32_e64 s[66:67], 5, v233
	v_cmp_eq_u32_e64 s[68:69], 6, v233
	v_cmp_eq_u32_e64 s[70:71], 7, v233
	v_cndmask_b32_e64 v248, v2, v3, s[64:65]
	v_cndmask_b32_e64 v249, v2, v3, s[66:67]
	v_cndmask_b32_e64 v250, v2, v3, s[68:69]
	v_cndmask_b32_e64 v251, v2, v3, s[70:71]
	v_mul_f32_e32 v248, v1, v248
	v_mul_f32_e32 v249, v1, v249
	v_mul_f32_e32 v250, v1, v250
	v_mul_f32_e32 v251, v1, v251
	v_cndmask_b32_e64 v248, v0, v248, s[2:3]
	v_cndmask_b32_e64 v249, v0, v249, s[2:3]
	v_cndmask_b32_e64 v250, v0, v250, s[2:3]
	v_cndmask_b32_e64 v251, v0, v251, s[2:3]
	v_mul_f32_e32 v248, v248, v182
	v_mul_f32_e32 v249, v249, v183
	v_mul_f32_e32 v250, v250, v178
	v_mul_f32_e32 v251, v251, v179
	ds_write_b128 v238, v[248:251] offset:32
	v_cmp_eq_u32_e64 s[64:65], 8, v233
	v_cmp_eq_u32_e64 s[66:67], 9, v233
	v_cmp_eq_u32_e64 s[68:69], 10, v233
	v_cmp_eq_u32_e64 s[70:71], 11, v233
	v_cndmask_b32_e64 v248, v2, v3, s[64:65]
	v_cndmask_b32_e64 v249, v2, v3, s[66:67]
	v_cndmask_b32_e64 v250, v2, v3, s[68:69]
	v_cndmask_b32_e64 v251, v2, v3, s[70:71]
	v_mul_f32_e32 v248, v1, v248
	v_mul_f32_e32 v249, v1, v249
	v_mul_f32_e32 v250, v1, v250
	v_mul_f32_e32 v251, v1, v251
	v_cndmask_b32_e64 v248, v0, v248, s[2:3]
	v_cndmask_b32_e64 v249, v0, v249, s[2:3]
	v_cndmask_b32_e64 v250, v0, v250, s[2:3]
	v_cndmask_b32_e64 v251, v0, v251, s[2:3]
	v_mul_f32_e32 v248, v248, v166
	v_mul_f32_e32 v249, v249, v167
	v_mul_f32_e32 v250, v250, v118
	v_mul_f32_e32 v251, v251, v119
	ds_write_b128 v238, v[248:251] offset:64
	v_cmp_eq_u32_e64 s[64:65], 12, v233
	v_cmp_eq_u32_e64 s[66:67], 13, v233
	v_cmp_eq_u32_e64 s[68:69], 14, v233
	v_cmp_eq_u32_e64 s[70:71], 15, v233
	v_cndmask_b32_e64 v248, v2, v3, s[64:65]
	v_cndmask_b32_e64 v249, v2, v3, s[66:67]
	v_cndmask_b32_e64 v250, v2, v3, s[68:69]
	v_cndmask_b32_e64 v251, v2, v3, s[70:71]
	v_mul_f32_e32 v248, v1, v248
	v_mul_f32_e32 v249, v1, v249
	v_mul_f32_e32 v250, v1, v250
	v_mul_f32_e32 v251, v1, v251
	v_cndmask_b32_e64 v248, v0, v248, s[2:3]
	v_cndmask_b32_e64 v249, v0, v249, s[2:3]
	v_cndmask_b32_e64 v250, v0, v250, s[2:3]
	v_cndmask_b32_e64 v251, v0, v251, s[2:3]
	v_mul_f32_e32 v248, v248, v116
	v_mul_f32_e32 v249, v249, v117
	v_mul_f32_e32 v250, v250, v114
	v_mul_f32_e32 v251, v251, v115
	ds_write_b128 v238, v[248:251] offset:96
	v_pk_mul_f32 v[248:249], v[0:1], v[112:113] op_sel_hi:[0,1]
	v_pk_mul_f32 v[250:251], v[0:1], v[98:99] op_sel_hi:[0,1]
	ds_write_b128 v238, v[248:251] offset:128
	v_pk_mul_f32 v[248:249], v[0:1], v[100:101] op_sel_hi:[0,1]
	v_pk_mul_f32 v[250:251], v[0:1], v[120:121] op_sel_hi:[0,1]
	ds_write_b128 v238, v[248:251] offset:160
	v_pk_mul_f32 v[248:249], v[0:1], v[102:103] op_sel_hi:[0,1]
	v_pk_mul_f32 v[250:251], v[0:1], v[122:123] op_sel_hi:[0,1]
	ds_write_b128 v238, v[248:251] offset:192
	v_pk_mul_f32 v[248:249], v[0:1], v[124:125] op_sel_hi:[0,1]
	v_pk_mul_f32 v[250:251], v[0:1], v[180:181] op_sel_hi:[0,1]
	ds_write_b128 v238, v[248:251] offset:224
	s_lshl_b32 s56, s56, 11
	s_add_i32 s56, s56, s25
	v_or_b32_e32 v252, s56, v239
	v_add_lshl_u32 v253, v241, s55, 7
	v_lshl_or_b32 v1, v252, 13, v240
	v_and_or_b32 v2, v253, s54, v1
	ds_read_b128 v[248:251], v246
	ds_read_b128 v[160:163], v246 offset:1088
	s_waitcnt lgkmcnt(1)
	global_store_dwordx4 v2, v[248:251], s[10:11] nt
	s_nop 0
	ds_read_b128 v[248:251], v246 offset:2176
	v_or_b32_e32 v3, 0x8000, v2
	s_waitcnt lgkmcnt(1)
	global_store_dwordx4 v3, v[160:163], s[10:11] nt
	s_nop 0
	ds_read_b128 v[160:163], v246 offset:3264
	v_or_b32_e32 v252, 0x10000, v2
	s_waitcnt lgkmcnt(1)
	global_store_dwordx4 v252, v[248:251], s[10:11] nt
	s_nop 0
	ds_read_b128 v[248:251], v246 offset:4352
	v_or_b32_e32 v3, 0x18000, v2
	s_waitcnt lgkmcnt(1)
	global_store_dwordx4 v3, v[160:163], s[10:11] nt
	s_nop 0
	ds_read_b128 v[160:163], v246 offset:5440
	v_or_b32_e32 v252, 0x20000, v2
	s_waitcnt lgkmcnt(1)
	global_store_dwordx4 v252, v[248:251], s[10:11] nt
	s_nop 0
	ds_read_b128 v[248:251], v246 offset:6528
	v_or_b32_e32 v3, 0x28000, v2
	s_waitcnt lgkmcnt(1)
	global_store_dwordx4 v3, v[160:163], s[10:11] nt
	s_nop 0
	ds_read_b128 v[160:163], v246 offset:7616
	v_or_b32_e32 v252, 0x30000, v2
	s_waitcnt lgkmcnt(1)
	global_store_dwordx4 v252, v[248:251], s[10:11] nt
	v_or_b32_e32 v3, 0x38000, v2
	s_waitcnt lgkmcnt(0)
	global_store_dwordx4 v3, v[160:163], s[10:11] nt
	v_pk_mul_f32 v[248:249], v[0:1], v[80:81] op_sel_hi:[0,1]
	v_pk_mul_f32 v[250:251], v[0:1], v[82:83] op_sel_hi:[0,1]
	ds_write_b128 v238, v[248:251]
	v_pk_mul_f32 v[248:249], v[0:1], v[84:85] op_sel_hi:[0,1]
	v_pk_mul_f32 v[250:251], v[0:1], v[96:97] op_sel_hi:[0,1]
	ds_write_b128 v238, v[248:251] offset:32
	v_pk_mul_f32 v[248:249], v[0:1], v[86:87] op_sel_hi:[0,1]
	v_pk_mul_f32 v[250:251], v[0:1], v[88:89] op_sel_hi:[0,1]
	ds_write_b128 v238, v[248:251] offset:64
	v_pk_mul_f32 v[248:249], v[0:1], v[90:91] op_sel_hi:[0,1]
	v_pk_mul_f32 v[250:251], v[0:1], v[94:95] op_sel_hi:[0,1]
	ds_write_b128 v238, v[248:251] offset:96
	v_pk_mul_f32 v[248:249], v[0:1], v[92:93] op_sel_hi:[0,1]
	v_pk_mul_f32 v[250:251], v[0:1], v[108:109] op_sel_hi:[0,1]
	ds_write_b128 v238, v[248:251] offset:128
	v_pk_mul_f32 v[248:249], v[0:1], v[110:111] op_sel_hi:[0,1]
	v_pk_mul_f32 v[250:251], v[0:1], v[176:177] op_sel_hi:[0,1]
	ds_write_b128 v238, v[248:251] offset:160
	v_pk_mul_f32 v[248:249], v[0:1], v[174:175] op_sel_hi:[0,1]
	v_pk_mul_f32 v[250:251], v[0:1], v[192:193] op_sel_hi:[0,1]
	ds_write_b128 v238, v[248:251] offset:192
	v_pk_mul_f32 v[248:249], v[0:1], v[194:195] op_sel_hi:[0,1]
	v_pk_mul_f32 v[250:251], v[0:1], v[206:207] op_sel_hi:[0,1]
	ds_write_b128 v238, v[248:251] offset:224
	v_add_u32_e32 v252, 0x100, v253
	v_and_or_b32 v2, v252, s54, v1
	ds_read_b128 v[248:251], v246
	ds_read_b128 v[160:163], v246 offset:1088
	s_waitcnt lgkmcnt(1)
	global_store_dwordx4 v2, v[248:251], s[10:11] nt
	s_nop 0
	ds_read_b128 v[248:251], v246 offset:2176
	v_or_b32_e32 v3, 0x8000, v2
	s_waitcnt lgkmcnt(1)
	global_store_dwordx4 v3, v[160:163], s[10:11] nt
	s_nop 0
	ds_read_b128 v[160:163], v246 offset:3264
	v_or_b32_e32 v252, 0x10000, v2
	s_waitcnt lgkmcnt(1)
	global_store_dwordx4 v252, v[248:251], s[10:11] nt
	s_nop 0
	ds_read_b128 v[248:251], v246 offset:4352
	v_or_b32_e32 v3, 0x18000, v2
	s_waitcnt lgkmcnt(1)
	global_store_dwordx4 v3, v[160:163], s[10:11] nt
	s_nop 0
	ds_read_b128 v[160:163], v246 offset:5440
	v_or_b32_e32 v252, 0x20000, v2
	s_waitcnt lgkmcnt(1)
	global_store_dwordx4 v252, v[248:251], s[10:11] nt
	s_nop 0
	ds_read_b128 v[248:251], v246 offset:6528
	v_or_b32_e32 v3, 0x28000, v2
	s_waitcnt lgkmcnt(1)
	global_store_dwordx4 v3, v[160:163], s[10:11] nt
	s_nop 0
	ds_read_b128 v[160:163], v246 offset:7616
	v_or_b32_e32 v252, 0x30000, v2
	s_waitcnt lgkmcnt(1)
	global_store_dwordx4 v252, v[248:251], s[10:11] nt
	v_or_b32_e32 v3, 0x38000, v2
	s_waitcnt lgkmcnt(0)
	global_store_dwordx4 v3, v[160:163], s[10:11] nt
	s_cmp_eq_u32 s12, 28
	s_cbranch_scc1 .Lkl_skip
	s_add_i32 s63, s62, 0x3000
	s_and_b32 s63, s63, 0x3f000
	s_or_b32 s63, s63, s58
	v_or_b32_e32 v2, s63, v231
	global_load_dwordx4 v[80:83], v2, s[6:7]
	global_load_dwordx4 v[84:87], v2, s[6:7] offset:1024
	global_load_dwordx4 v[88:91], v2, s[6:7] offset:2048
	global_load_dwordx4 v[92:95], v2, s[6:7] offset:3072
	s_add_i32 s63, s62, 0x2000
	s_and_b32 s63, s63, 0x3f000
	s_or_b32 s63, s63, s58
	v_or_b32_e32 v3, s63, v231
	global_load_dwordx4 v[96:99], v3, s[6:7]
	global_load_dwordx4 v[100:103], v3, s[6:7] offset:1024
	global_load_dwordx4 v[108:111], v3, s[6:7] offset:2048
	global_load_dwordx4 v[192:195], v3, s[6:7] offset:3072
	s_add_i32 s63, s62, 0x1000
	s_and_b32 s63, s63, 0x3f000
	s_or_b32 s63, s63, s58
	v_or_b32_e32 v2, s63, v231
	global_load_dwordx4 v[174:177], v2, s[6:7] offset:2048
	global_load_dwordx4 v[178:181], v2, s[6:7] offset:3072
.Lkl_skip:
	v_pk_mul_f32 v[248:249], v[0:1], v[64:65] op_sel_hi:[0,1]
	v_pk_mul_f32 v[250:251], v[0:1], v[66:67] op_sel_hi:[0,1]
	ds_write_b128 v238, v[248:251]
	v_pk_mul_f32 v[248:249], v[0:1], v[68:69] op_sel_hi:[0,1]
	v_pk_mul_f32 v[250:251], v[0:1], v[74:75] op_sel_hi:[0,1]
	ds_write_b128 v238, v[248:251] offset:32
	v_pk_mul_f32 v[248:249], v[0:1], v[72:73] op_sel_hi:[0,1]
	v_pk_mul_f32 v[250:251], v[0:1], v[104:105] op_sel_hi:[0,1]
	ds_write_b128 v238, v[248:251] offset:64
	v_pk_mul_f32 v[248:249], v[0:1], v[106:107] op_sel_hi:[0,1]
	v_pk_mul_f32 v[250:251], v[0:1], v[172:173] op_sel_hi:[0,1]
	ds_write_b128 v238, v[248:251] offset:96
	v_pk_mul_f32 v[248:249], v[0:1], v[170:171] op_sel_hi:[0,1]
	v_pk_mul_f32 v[250:251], v[0:1], v[188:189] op_sel_hi:[0,1]
	ds_write_b128 v238, v[248:251] offset:128
	v_pk_mul_f32 v[248:249], v[0:1], v[190:191] op_sel_hi:[0,1]
	v_pk_mul_f32 v[250:251], v[0:1], v[202:203] op_sel_hi:[0,1]
	ds_write_b128 v238, v[248:251] offset:160
	v_pk_mul_f32 v[248:249], v[0:1], v[200:201] op_sel_hi:[0,1]
	v_pk_mul_f32 v[250:251], v[0:1], v[214:215] op_sel_hi:[0,1]
	ds_write_b128 v238, v[248:251] offset:192
	v_pk_mul_f32 v[248:249], v[0:1], v[216:217] op_sel_hi:[0,1]
	v_pk_mul_f32 v[250:251], v[0:1], v[222:223] op_sel_hi:[0,1]
	ds_write_b128 v238, v[248:251] offset:224
	v_add_u32_e32 v252, 0x200, v253
	v_and_or_b32 v2, v252, s54, v1
	ds_read_b128 v[248:251], v246
	ds_read_b128 v[160:163], v246 offset:1088
	s_waitcnt lgkmcnt(1)
	global_store_dwordx4 v2, v[248:251], s[10:11] nt
	s_nop 0
	ds_read_b128 v[248:251], v246 offset:2176
	v_or_b32_e32 v3, 0x8000, v2
	s_waitcnt lgkmcnt(1)
	global_store_dwordx4 v3, v[160:163], s[10:11] nt
	s_nop 0
	ds_read_b128 v[160:163], v246 offset:3264
	v_or_b32_e32 v252, 0x10000, v2
	s_waitcnt lgkmcnt(1)
	global_store_dwordx4 v252, v[248:251], s[10:11] nt
	s_nop 0
	ds_read_b128 v[248:251], v246 offset:4352
	v_or_b32_e32 v3, 0x18000, v2
	s_waitcnt lgkmcnt(1)
	global_store_dwordx4 v3, v[160:163], s[10:11] nt
	s_nop 0
	ds_read_b128 v[160:163], v246 offset:5440
	v_or_b32_e32 v252, 0x20000, v2
	s_waitcnt lgkmcnt(1)
	global_store_dwordx4 v252, v[248:251], s[10:11] nt
	s_nop 0
	ds_read_b128 v[248:251], v246 offset:6528
	v_or_b32_e32 v3, 0x28000, v2
	s_waitcnt lgkmcnt(1)
	global_store_dwordx4 v3, v[160:163], s[10:11] nt
	s_nop 0
	ds_read_b128 v[160:163], v246 offset:7616
	v_or_b32_e32 v252, 0x30000, v2
	s_waitcnt lgkmcnt(1)
	global_store_dwordx4 v252, v[248:251], s[10:11] nt
	v_or_b32_e32 v3, 0x38000, v2
	s_waitcnt lgkmcnt(0)
	global_store_dwordx4 v3, v[160:163], s[10:11] nt
	v_pk_mul_f32 v[248:249], v[0:1], v[70:71] op_sel_hi:[0,1]
	v_pk_mul_f32 v[250:251], v[0:1], v[76:77] op_sel_hi:[0,1]
	ds_write_b128 v238, v[248:251]
	v_pk_mul_f32 v[248:249], v[0:1], v[78:79] op_sel_hi:[0,1]
	v_pk_mul_f32 v[250:251], v[0:1], v[168:169] op_sel_hi:[0,1]
	ds_write_b128 v238, v[248:251] offset:32
	v_pk_mul_f32 v[248:249], v[0:1], v[126:127] op_sel_hi:[0,1]
	v_pk_mul_f32 v[250:251], v[0:1], v[184:185] op_sel_hi:[0,1]
	ds_write_b128 v238, v[248:251] offset:64
	v_pk_mul_f32 v[248:249], v[0:1], v[186:187] op_sel_hi:[0,1]
	v_pk_mul_f32 v[250:251], v[0:1], v[198:199] op_sel_hi:[0,1]
	ds_write_b128 v238, v[248:251] offset:96
	v_pk_mul_f32 v[248:249], v[0:1], v[196:197] op_sel_hi:[0,1]
	v_pk_mul_f32 v[250:251], v[0:1], v[210:211] op_sel_hi:[0,1]
	ds_write_b128 v238, v[248:251] offset:128
	v_pk_mul_f32 v[248:249], v[0:1], v[212:213] op_sel_hi:[0,1]
	v_pk_mul_f32 v[250:251], v[0:1], v[220:221] op_sel_hi:[0,1]
	ds_write_b128 v238, v[248:251] offset:160
	v_pk_mul_f32 v[248:249], v[0:1], v[218:219] op_sel_hi:[0,1]
	v_pk_mul_f32 v[250:251], v[0:1], v[224:225] op_sel_hi:[0,1]
	ds_write_b128 v238, v[248:251] offset:192
	v_pk_mul_f32 v[248:249], v[0:1], v[226:227] op_sel_hi:[0,1]
	v_pk_mul_f32 v[250:251], v[0:1], v[228:229] op_sel_hi:[0,1]
	ds_write_b128 v238, v[248:251] offset:224
	v_add_u32_e32 v252, 0x300, v253
	v_and_or_b32 v2, v252, s54, v1
	ds_read_b128 v[248:251], v246
	ds_read_b128 v[160:163], v246 offset:1088
	s_waitcnt lgkmcnt(1)
	global_store_dwordx4 v2, v[248:251], s[10:11] nt
	s_nop 0
	ds_read_b128 v[248:251], v246 offset:2176
	v_or_b32_e32 v3, 0x8000, v2
	s_waitcnt lgkmcnt(1)
	global_store_dwordx4 v3, v[160:163], s[10:11] nt
	s_nop 0
	ds_read_b128 v[160:163], v246 offset:3264
	v_or_b32_e32 v252, 0x10000, v2
	s_waitcnt lgkmcnt(1)
	global_store_dwordx4 v252, v[248:251], s[10:11] nt
	s_nop 0
	ds_read_b128 v[248:251], v246 offset:4352
	v_or_b32_e32 v3, 0x18000, v2
	s_waitcnt lgkmcnt(1)
	global_store_dwordx4 v3, v[160:163], s[10:11] nt
	s_nop 0
	ds_read_b128 v[160:163], v246 offset:5440
	v_or_b32_e32 v252, 0x20000, v2
	s_waitcnt lgkmcnt(1)
	global_store_dwordx4 v252, v[248:251], s[10:11] nt
	s_nop 0
	ds_read_b128 v[248:251], v246 offset:6528
	v_or_b32_e32 v3, 0x28000, v2
	s_waitcnt lgkmcnt(1)
	global_store_dwordx4 v3, v[160:163], s[10:11] nt
	s_nop 0
	ds_read_b128 v[160:163], v246 offset:7616
	v_or_b32_e32 v252, 0x30000, v2
	s_waitcnt lgkmcnt(1)
	global_store_dwordx4 v252, v[248:251], s[10:11] nt
	v_or_b32_e32 v3, 0x38000, v2
	s_waitcnt lgkmcnt(0)
	global_store_dwordx4 v3, v[160:163], s[10:11] nt
	s_mov_b32 s57, s24
	s_add_i32 s12, s12, 4
	s_cmp_eq_u32 s12, 32
	s_cbranch_scc1 .LBB1_22
